# prefetched residual loads in mix-out and PV epilogues; hoisted row-scale loads and async next-unit index loads in the MoE GEMMs; conflict-free LDS layout for the router weights
# speedup vs baseline: 1.0166x; 1.0166x over previous
; __device__ __forceinline__ void phase2(const int WID_, const char* items, float* Y, char* lds, const int vblk, const int nvblk) {
;     ...
;         if (upd) __builtin_amdgcn_s_setprio(3);
;         for (int c = 0; c < S / 64; c += 8) {
;             P2_STEP(1, c); P2_STEP(2, c + 1); P2_STEP(3, c + 2); P2_STEP(4, c + 3); P2_STEP(5, c + 4); P2_STEP(6, c + 5); P2_STEP(7, c + 6); P2_STEP(0, c + 7);
.LBB0_1616:
	s_waitcnt lgkmcnt(0)
	s_barrier
	s_mov_b64 s[40:41], 0x100000
	s_add_i32 s47, s47, 8
	v_lshl_add_u64 v[126:127], v[126:127], 0, s[22:23]
	v_lshl_add_u64 v[128:129], v[128:129], 0, s[22:23]
	v_lshl_add_u64 v[130:131], v[130:131], 0, s[40:41]
	s_and_b64 vcc, exec, s[38:39]
	s_cbranch_vccnz .LBB0_1606
.LBB0_1617:
	ds_read2st64_b64 v[120:123], v124 offset0:56 offset1:57
	ds_read_b128 v[100:103], v140 offset:10240
	ds_read_b128 v[96:99], v140 offset:10304
	ds_read_b128 v[116:119], v138
	ds_read_b128 v[104:107], v138 offset:64
	ds_read_b128 v[112:115], v138 offset:2304
	ds_read_b128 v[108:111], v138 offset:2368
	s_cmpk_gt_u32 s47, 0x76
	v_lshl_add_u64 v[134:135], v[126:127], 0, s[36:37]
	v_lshl_add_u64 v[132:133], v[128:129], 0, s[36:37]
	s_waitcnt vmcnt(2)
	ds_write_b128 v136, v[0:3] offset:36864
	s_waitcnt vmcnt(1)
	ds_write_b128 v136, v[4:7] offset:46080
	s_waitcnt vmcnt(0)
	ds_write_b128 v137, v[12:15] offset:55296
	s_cbranch_scc1 .LBB0_1619
	v_add_co_u32_e32 v0, vcc, 0x48000, v134
	s_nop 1
	v_addc_co_u32_e32 v1, vcc, 0, v135, vcc
	v_add_co_u32_e32 v4, vcc, 0x4a000, v134
	s_nop 1
	v_addc_co_u32_e32 v5, vcc, 0, v135, vcc
	v_add_co_u32_e32 v12, vcc, 0x4c000, v132
	global_load_dwordx4 v[0:3], v[0:1], off
	s_nop 0
	global_load_dwordx4 v[4:7], v[4:5], off
	v_addc_co_u32_e32 v13, vcc, 0, v133, vcc
	global_load_dwordx4 v[12:15], v[12:13], off

; __device__ __forceinline__ void router_ph(const int WID_, const bf16* __restrict__ x3, const float* __restrict__ nw, const float* __restrict__ wrg, const float* __restrict__ brg, ...
;     ...
;     for (int i = wv * 64 + lane; i < 1024; i += NT) { const float4 w = *(const float4*)(wrg + i * 4);
;         typedef _Float16 h4 __attribute__((ext_vector_type(4))); *(h4*)(wg16 + i * 4) = (h4){(_Float16)w.x, (_Float16)w.y, (_Float16)w.z, (_Float16)w.w}; }
.LBB0_2133:
	s_or_b64 exec, exec, s[2:3]
	v_add_u32_e32 v1, s86, v20
	v_readlane_b32 s0, v243, 61
	v_cmp_gt_i32_e32 vcc, s50, v1
	v_add_u32_e32 v4, s47, v20
	v_lshl_add_u32 v0, v20, 2, s0
	s_and_saveexec_b64 s[2:3], vcc
	v_readlane_b32 s8, v242, 15
	v_readlane_b32 s10, v242, 17
	v_readlane_b32 s11, v242, 18
	v_readlane_b32 s9, v242, 16
	v_readlane_b32 s12, v242, 19
	v_readlane_b32 s13, v242, 20
	v_readlane_b32 s14, v242, 21
	v_readlane_b32 s15, v242, 22
	v_readlane_b32 s16, v242, 23
	v_readlane_b32 s17, v242, 24
	v_readlane_b32 s18, v242, 25
	v_readlane_b32 s19, v242, 26
	v_readlane_b32 s20, v242, 27
	v_readlane_b32 s21, v242, 28
	v_readlane_b32 s22, v242, 29
	v_readlane_b32 s23, v242, 30
	s_cbranch_execz .LBB0_2136
	v_readlane_b32 s0, v242, 46
	v_add_u32_e32 v5, s47, v20
	s_mov_b64 s[4:5], 0
	v_and_b32_e32 v6, 6, v1
	v_lshlrev_b32_e32 v6, 9, v6
	v_lshrrev_b32_e32 v7, 3, v1
	v_lshl_add_u32 v6, v7, 4, v6
	v_and_b32_e32 v7, 1, v1
	v_lshl_add_u32 v6, v7, 3, v6
	v_add_u32_e32 v6, 0x100, v6
	v_readlane_b32 s0, v243, 61
	s_nop 1
	v_lshl_add_u32 v2, v20, 2, s0

; __device__ __forceinline__ void pin4(float4& v) { asm volatile("" : "+v"(v.x), "+v"(v.y), "+v"(v.z), "+v"(v.w)); }
; __device__ __forceinline__ void router_ph(const int WID_, const bf16* __restrict__ x3, const float* __restrict__ nw, const float* __restrict__ wrg, const float* __restrict__ brg, ...
;     ...
;     for (int i = wv * 64 + lane; i < 4 * 1024 * 2; i += NT) { const float4 w = *(const float4*)(wre + i * 4);
;         typedef _Float16 h4 __attribute__((ext_vector_type(4))); *(h4*)(we16 + i * 4) = (h4){(_Float16)w.x, (_Float16)w.y, (_Float16)w.z, (_Float16)w.w}; }
;     __syncthreads();
;     typedef _Float16 h4 __attribute__((ext_vector_type(4)));
;     typedef _Float16 h8 __attribute__((ext_vector_type(8)));
;     float4 gw[4];
; #pragma unroll
;     for (int j = 0; j < 2; ++j) { gw[2 * j] = *(const float4*)(nw + (lane + 64 * j) * 8); gw[2 * j + 1] = *(const float4*)(nw + (lane + 64 * j) * 8 + 4); }
;     uint4 nx[2];
; #pragma unroll
;     for (int j = 0; j < 2; ++j) nx[j] = ((const uint4*)(x3 + (size_t)(tile * 256 + wv) * D))[lane + 64 * j];
; #pragma unroll
;     for (int j = 0; j < 4; ++j) pg8::pin4(gw[j]);
; #pragma unroll
;     for (int j = 0; j < 2; ++j) asm volatile("" : "+v"(nx[j].x), "+v"(nx[j].y), "+v"(nx[j].z), "+v"(nx[j].w));
.LBB0_2136:
	s_or_b64 exec, exec, s[2:3]
	s_movk_i32 s2, 0x1fff
	v_cmp_lt_i32_e32 vcc, s2, v1
	v_lshlrev_b32_e32 v22, 3, v20
	s_and_saveexec_b64 s[2:3], vcc
	s_xor_b64 s[2:3], exec, s[2:3]
	v_lshlrev_b32_e32 v22, 3, v20
	s_andn2_saveexec_b64 s[2:3], s[2:3]
	s_cbranch_execz .LBB0_2142
	v_readlane_b32 s0, v242, 47
	v_readlane_b32 s8, v242, 15
	s_mov_b64 s[4:5], 0
	v_bfe_u32 v2, v1, 1, 3
	v_lshlrev_b32_e32 v2, 10, v2
	v_lshrrev_b32_e32 v3, 4, v1
	v_lshl_add_u32 v2, v3, 4, v2
	v_and_b32_e32 v3, 1, v1
	v_lshl_add_u32 v2, v3, 3, v2
	v_add_u32_e32 v2, 0x2100, v2
	s_movk_i32 s98, 0x200
	v_readlane_b32 s14, v242, 21
	v_readlane_b32 s15, v242, 22
	v_readlane_b32 s9, v242, 16
	v_readlane_b32 s10, v242, 17
	v_readlane_b32 s11, v242, 18
	v_readlane_b32 s12, v242, 19
	v_readlane_b32 s13, v242, 20
	v_readlane_b32 s16, v242, 23
	v_readlane_b32 s17, v242, 24
	v_readlane_b32 s18, v242, 25
	v_readlane_b32 s19, v242, 26
	v_readlane_b32 s20, v242, 27
	v_readlane_b32 s21, v242, 28
	v_readlane_b32 s22, v242, 29
	v_readlane_b32 s23, v242, 30
.LBB0_2140:
	v_ashrrev_i32_e32 v1, 31, v0
	v_lshl_add_u64 v[6:7], v[0:1], 2, s[14:15]
	global_load_dwordx4 v[6:9], v[6:7], off
	v_add_u32_e32 v4, 0x200, v4
	s_movk_i32 s6, 0x1dff
	v_cmp_lt_i32_e32 vcc, s6, v4
	v_add_u32_e32 v0, 0x800, v0
	s_or_b64 s[4:5], vcc, s[4:5]
	s_waitcnt vmcnt(0)
	v_cvt_f16_f32_e32 v1, v6
	v_cvt_f16_f32_e32 v3, v9
	v_cvt_pk_f16_f32 v5, v7, v8
	v_pack_b32_f16 v6, v1, v5
	v_alignbit_b32 v7, v3, v5, 16
	ds_write_b64 v2, v[6:7]
	v_add_u32_e32 v2, s98, v2
	s_xor_b32 s98, s98, 0x1c00
	s_andn2_b64 exec, exec, s[4:5]
	s_cbranch_execnz .LBB0_2140
	s_or_b64 exec, exec, s[4:5]
.LBB0_2142:
	s_or_b64 exec, exec, s[2:3]
	v_readlane_b32 s0, v242, 15
	v_readlane_b32 s2, v242, 17
	v_readlane_b32 s6, v242, 21
	v_readlane_b32 s4, v242, 19
	s_lshl_b32 s6, s42, 8
	v_readlane_b32 s2, v243, 44
	v_readlane_b32 s5, v242, 20
	s_add_i32 s4, s6, s2
	v_readlane_b32 s3, v242, 18
	s_ashr_i32 s5, s4, 31
	s_lshl_b64 s[2:3], s[4:5], 11
	v_ashrrev_i32_e32 v23, 31, v22
	v_readlane_b32 s1, v242, 16
	s_add_u32 s2, s92, s2
	s_addc_u32 s3, s93, s3
	v_lshl_add_u64 v[12:13], v[22:23], 2, s[0:1]
	s_waitcnt lgkmcnt(0)
	s_barrier
	global_load_dwordx4 v[0:3], v[12:13], off
	global_load_dwordx4 v[4:7], v[12:13], off offset:16
	global_load_dwordx4 v[8:11], v[12:13], off offset:2048
	global_load_dwordx4 v[24:27], v[12:13], off offset:2064
	v_lshl_add_u64 v[12:13], v[20:21], 4, s[2:3]
	global_load_dwordx4 v[16:19], v[12:13], off
	s_nop 0
	global_load_dwordx4 v[12:15], v[12:13], off offset:1024
	v_readlane_b32 s0, v243, 42
	v_readlane_b32 s1, v243, 43
	s_and_b64 vcc, exec, s[0:1]
	v_readlane_b32 s7, v242, 22
	v_readlane_b32 s8, v242, 23
	v_readlane_b32 s9, v242, 24
	v_readlane_b32 s10, v242, 25
	v_readlane_b32 s11, v242, 26
	v_readlane_b32 s12, v242, 27
	v_readlane_b32 s13, v242, 28
	v_readlane_b32 s14, v242, 29
	v_readlane_b32 s15, v242, 30
	s_waitcnt vmcnt(5)
	v_mov_b32_e32 v29, v0
	v_mov_b32_e32 v30, v2
	v_mov_b32_e32 v31, v1
	s_waitcnt vmcnt(4)
	v_mov_b32_e32 v32, v5
	v_mov_b32_e32 v33, v4
	s_waitcnt vmcnt(3)
	v_mov_b32_e32 v34, v11
	v_mov_b32_e32 v35, v10
	s_waitcnt vmcnt(2)
	v_mov_b32_e32 v1, v24
	v_mov_b32_e32 v5, v26
	v_mov_b32_e32 v0, v25
	v_mov_b32_e32 v4, v27
	s_waitcnt vmcnt(0)
	v_mov_b32_e32 v2, v14
	s_cbranch_vccz .LBB0_2150
	s_add_i32 s33, s4, 0xf8
	s_or_b32 s43, s6, 0xf8
	s_lshl_b64 s[4:5], s[4:5], 2
	v_readlane_b32 s0, v242, 43
	v_readlane_b32 s1, v242, 44
	s_add_u32 s78, s0, s4
	v_add_u32_e32 v10, 0x200, v22
	v_or_b32_e32 v11, 2, v22
	v_or_b32_e32 v24, 4, v22
	v_or_b32_e32 v26, 6, v22
	v_add_u32_e32 v46, 0x202, v22
	v_add_u32_e32 v48, 0x204, v22
	v_add_u32_e32 v50, 0x206, v22
	s_addc_u32 s79, s1, s5
	s_lshl_b32 s4, s42, 9
	v_readlane_b32 s0, v242, 48
	v_lshlrev_b32_e32 v14, 6, v20
	v_lshlrev_b32_e32 v23, 3, v11
	v_lshlrev_b32_e32 v25, 3, v24
	v_lshlrev_b32_e32 v27, 3, v26
	v_lshlrev_b32_e32 v55, 3, v10
	v_lshlrev_b32_e32 v56, 3, v46
	v_lshlrev_b32_e32 v57, 3, v48
	v_lshlrev_b32_e32 v58, 3, v50
	v_lshlrev_b32_e32 v22, 4, v22
	s_add_i32 s80, s0, s4
	v_readlane_b32 s0, v242, 49
	v_cmp_eq_u32_e64 s[2:3], 0, v20
	v_lshlrev_b32_e32 v36, 7, v20
	v_or_b32_e32 v37, 16, v22
	v_lshlrev_b32_e32 v38, 4, v11
	v_or_b32_e32 v39, 48, v22
	v_lshlrev_b32_e32 v40, 4, v24
	v_or_b32_e32 v41, 0x50, v22
	v_lshlrev_b32_e32 v42, 4, v26
	v_or_b32_e32 v43, 0x70, v22
	v_lshlrev_b32_e32 v44, 4, v10
	v_add_u32_e32 v45, 0x2010, v22
	v_lshlrev_b32_e32 v46, 4, v46
	v_add_u32_e32 v47, 0x2030, v22
	v_lshlrev_b32_e32 v48, 4, v48
	v_add_u32_e32 v49, 0x2050, v22
	v_lshlrev_b32_e32 v50, 4, v50
	v_add_u32_e32 v51, 0x2070, v22
	v_lshl_add_u64 v[10:11], v[20:21], 4, s[92:93]
	s_add_i32 s44, s0, s6
	v_add_u32_e32 v21, 0, v14
	v_add_u32_e32 v52, 0, v23
	v_add_u32_e32 v53, 0, v25
	v_add_u32_e32 v54, 0, v27
	v_add_u32_e32 v55, 0, v55
	v_add_u32_e32 v56, 0, v56
	v_add_u32_e32 v57, 0, v57
	v_add_u32_e32 v58, 0, v58
	v_lshlrev_b32_e32 v36, 4, v20
	v_add_u32_e32 v37, 0x400, v36
	v_add_u32_e32 v38, 0x800, v36
	v_add_u32_e32 v39, 0xc00, v36
	v_add_u32_e32 v40, 0x1000, v36
	v_add_u32_e32 v41, 0x1400, v36
	v_add_u32_e32 v42, 0x1800, v36
	v_add_u32_e32 v43, 0x1c00, v36
	v_add_u32_e32 v44, 0x2000, v36
	v_add_u32_e32 v45, 0x2400, v36
	v_add_u32_e32 v46, 0x2800, v36
	v_add_u32_e32 v47, 0x2c00, v36
	v_add_u32_e32 v48, 0x3000, v36
	v_add_u32_e32 v49, 0x3400, v36
	v_add_u32_e32 v50, 0x3800, v36
	v_add_u32_e32 v51, 0x3c00, v36
	v_mov_b32_e32 v21, v36
	v_mov_b32_e32 v52, v37
	v_mov_b32_e32 v53, v38
	v_mov_b32_e32 v54, v39
	v_mov_b32_e32 v55, v40
	v_mov_b32_e32 v56, v41
	v_mov_b32_e32 v57, v42
	v_mov_b32_e32 v58, v43
	s_branch .LBB0_2145

;     __device__ __forceinline__ const char* aptr(const Unit& u) const { return (const char*)(A + (size_t)u.pm * BM * lda); }
;     __device__ __forceinline__ const char* bptr(const Unit& u) const { return (const char*)(Bt + (size_t)u.pn * BM * ldb); }
;     __device__ __forceinline__ const char* aptr(const Unit& u) const { return (const char*)(A + (size_t)u.pm * BM * lda + koff(u)); }
;     __device__ __forceinline__ const char* bptr(const Unit& u) const { return (const char*)(Bt + (size_t)u.pn * BM * ldb + koff(u)); }
;     __device__ bool next(int i, Unit& u) const { if (i >= 6) return false; int pm_ = pm; asm volatile("" : "+s"(pm_)); u.pm = pm_; u.pn = (i + (GB >> 3)) % 6; return true; }
;     __device__ __forceinline__ const char* aptr(const Unit& u) const { return (const char*)(A + (size_t)u.pm * BM * lda + koff(u)); }
;     __device__ __forceinline__ const char* bptr(const Unit& u) const { return (const char*)(Bt + (size_t)u.pn * BM * ldb + koff(u)); }
; #define PG8_GOFF(dst, u) do { if constexpr (GA) { _Pragma("unroll") for (int h_ = 0; h_ < 2; ++h_) _Pragma("unroll") for (int i_ = 0; i_ < 2; ++i_) \
;         dst[h_][i_] = (unsigned)(S.grow(u, h_ * HALF + gR[i_]) * S.lda + gC[i_]) * 2u; } } while (0)
;     __device__ __forceinline__ const char* aptr(const Unit& u) const { const int g = u.pm / nM, pm = u.pm % nM; return (const char*)(A + (size_t)g * sA + (size_t)pm * BM * lda); }
; template <class Epi, class Sched>
; __device__ __forceinline__ void gemm_phase(const int WID_, PG8_LAS unsigned char* lds, const Sched& S, const Epi& E) {
;     ...
;         const bool has_next = S.next(ui + 1, nxt);
;         const char* nA = has_next ? S.aptr(nxt) : cA; const char* nB = has_next ? S.bptr(nxt) : cB;
;         if (has_next) PG8_GOFF(vgn, nxt); else { if constexpr (GA) { _Pragma("unroll") for (int h_ = 0; h_ < 2; ++h_) _Pragma("unroll") for (int i_ = 0; i_ < 2; ++i_) vgn[h_][i_] = vgc[h_][i_]; } }
;     __device__ bool next(int i, Unit& u) const { const int L = i * G + c; if (L >= nunits) return false; u.pm = L >> 2; u.pn = L & 3; return true; }
;     __device__ __forceinline__ const char* bptr(const Unit& u) const { const int e = __hip_atomic_load(tiles + u.pm, __ATOMIC_RELAXED, __HIP_MEMORY_SCOPE_AGENT); return (const char*)(Bt + ((size_t)e * bexp + (size_t)u.pn * BM) * ldb); }
.LBB0_2289:
	s_mov_b32 s99, 0
	s_add_i32 s48, s48, 1
	s_mul_i32 s0, s48, s94
	s_add_i32 s0, s0, s68
	s_cmp_lt_i32 s0, s34
	s_cselect_b64 s[4:5], -1, 0
	s_and_b32 s64, s0, 3
	s_ashr_i32 s44, s0, 2
	s_cmp_ge_i32 s0, s34
	s_cbranch_scc1 .LBB0_2291
	s_ashr_i32 s45, s44, 31
	s_lshl_b64 s[0:1], s[44:45], 2
	s_add_u32 s0, s16, s0
	s_addc_u32 s1, s17, s1
	global_load_dword v234, v133, s[0:1] sc1
	s_mov_b32 s99, 1
.LBB0_2291:
	v_cndmask_b32_e64 v0, 0, 1, s[4:5]
	v_cmp_ne_u32_e64 s[0:1], 1, v0
	s_andn2_b64 vcc, exec, s[4:5]
	v_mov_b32_e32 v157, v134
	v_mov_b32_e32 v158, v136
	v_mov_b32_e32 v159, v138
	v_mov_b32_e32 v160, v140
	s_cbranch_vccnz .LBB0_2293
	s_lshl_b32 s4, s44, 8
	v_add_u32_e32 v0, s4, v146
	v_add_u32_e32 v2, s4, v147
	s_bitset1_b32 s4, 7
	v_ashrrev_i32_e32 v1, 31, v0
	v_ashrrev_i32_e32 v3, 31, v2
	v_add_u32_e32 v4, s4, v146
	v_add_u32_e32 v6, s4, v147
	v_lshl_add_u64 v[0:1], v[0:1], 2, s[22:23]
	v_lshl_add_u64 v[2:3], v[2:3], 2, s[22:23]
	v_ashrrev_i32_e32 v5, 31, v4
	v_ashrrev_i32_e32 v7, 31, v6
	v_lshl_add_u64 v[4:5], v[4:5], 2, s[22:23]
	v_lshl_add_u64 v[6:7], v[6:7], 2, s[22:23]
	global_load_dword v235, v[0:1], off
	s_nop 0
	global_load_dword v236, v[2:3], off
	s_nop 0
	global_load_dword v237, v[4:5], off
	global_load_dword v238, v[6:7], off

;     __device__ __forceinline__ const char* bptr(const Unit& u) const { return (const char*)(Bt + (size_t)u.pn * BM * ldb); }
;     __device__ __forceinline__ const char* bptr(const Unit& u) const { return (const char*)(Bt + (size_t)u.pn * BM * ldb + koff(u)); }
;     __device__ bool next(int i, Unit& u) const { if (i >= 6) return false; int pm_ = pm; asm volatile("" : "+s"(pm_)); u.pm = pm_; u.pn = (i + (GB >> 3)) % 6; return true; }
;     __device__ __forceinline__ const char* bptr(const Unit& u) const { return (const char*)(Bt + (size_t)u.pn * BM * ldb + koff(u)); }
;     __device__ __forceinline__ const char* bptr(const Unit& u) const { const int g = u.pm / nM; return (const char*)(Bt + (size_t)g * sB + (size_t)u.pn * BM * ldb); }
;     __device__ bool next(int i, Unit& u) const { if (i >= nN) return false; int pm_ = pm; asm volatile("" : "+s"(pm_)); u.pm = pm_; u.pn = (i + (GB >> 3)) & (nN - 1); return true; }
;     __device__ __forceinline__ const char* bptr(const Unit& u) const { return (const char*)(Bt + (size_t)u.pn * BM * ldb); }
;     __device__ bool next(int i, Unit& u) const { const int L = i * G + c; if (L >= nunits) return false; u.pm = L >> 2; u.pn = L & 3; return true; }
;     __device__ __forceinline__ const char* bptr(const Unit& u) const { const int e = __hip_atomic_load(tiles + u.pm, __ATOMIC_RELAXED, __HIP_MEMORY_SCOPE_AGENT); return (const char*)(Bt + ((size_t)e * bexp + (size_t)u.pn * BM) * ldb); }
.LBB0_2294:
	s_cmpk_eq_i32 s4, 0x300
	s_cbranch_scc0 .Lg1_nofix
	s_cmp_eq_u32 s99, 0
	s_cbranch_scc1 .Lg1_nofix
	v_readfirstlane_b32 s100, v234
	s_lshl_b32 s98, s64, 19
	s_ashr_i32 s101, s100, 31
	s_lshl_b64 s[100:101], s[100:101], 21
	s_add_u32 s100, s28, s100
	s_addc_u32 s101, s29, s101
	s_add_u32 s42, s100, s98
	s_addc_u32 s43, s101, 0
	v_lshl_add_u32 v157, v235, 11, v148
	v_lshl_add_u32 v158, v236, 11, v149
	v_lshl_add_u32 v159, v237, 11, v148
	v_lshl_add_u32 v160, v238, 11, v149

;     __device__ __forceinline__ const char* aptr(const Unit& u) const { return (const char*)(A + (size_t)u.pm * BM * lda); }
;     __device__ __forceinline__ const char* bptr(const Unit& u) const { return (const char*)(Bt + (size_t)u.pn * BM * ldb); }
;     __device__ __forceinline__ const char* aptr(const Unit& u) const { return (const char*)(A + (size_t)u.pm * BM * lda + koff(u)); }
;     __device__ __forceinline__ const char* bptr(const Unit& u) const { return (const char*)(Bt + (size_t)u.pn * BM * ldb + koff(u)); }
;     __device__ bool next(int i, Unit& u) const { if (i >= 6) return false; int pm_ = pm; asm volatile("" : "+s"(pm_)); u.pm = pm_; u.pn = (i + (GB >> 3)) % 6; return true; }
;     __device__ __forceinline__ const char* aptr(const Unit& u) const { return (const char*)(A + (size_t)u.pm * BM * lda + koff(u)); }
;     __device__ __forceinline__ const char* bptr(const Unit& u) const { return (const char*)(Bt + (size_t)u.pn * BM * ldb + koff(u)); }
;     __device__ __forceinline__ const char* aptr(const Unit& u) const { const int g = u.pm / nM, pm = u.pm % nM; return (const char*)(A + (size_t)g * sA + (size_t)pm * BM * lda); }
;     __device__ __forceinline__ const char* bptr(const Unit& u) const { const int g = u.pm / nM; return (const char*)(Bt + (size_t)g * sB + (size_t)u.pn * BM * ldb); }
;     __device__ bool next(int i, Unit& u) const { if (i >= nN) return false; int pm_ = pm; asm volatile("" : "+s"(pm_)); u.pm = pm_; u.pn = (i + (GB >> 3)) & (nN - 1); return true; }
;     __device__ __forceinline__ const char* aptr(const Unit& u) const { return (const char*)(A + (size_t)u.pm * BM * lda); }
; template <class Epi, class Sched>
; __device__ __forceinline__ void gemm_phase(const int WID_, PG8_LAS unsigned char* lds, const Sched& S, const Epi& E) {
;     ...
;         const bool has_next = S.next(ui + 1, nxt);
;         const char* nA = has_next ? S.aptr(nxt) : cA; const char* nB = has_next ? S.bptr(nxt) : cB;
;     __device__ bool next(int i, Unit& u) const { const int L = i * G + c; if (L >= nunits) return false; u.pm = L >> 2; u.pn = L & 3; return true; }
;     __device__ __forceinline__ const char* bptr(const Unit& u) const { const int e = __hip_atomic_load(tiles + u.pm, __ATOMIC_RELAXED, __HIP_MEMORY_SCOPE_AGENT); return (const char*)(Bt + ((size_t)e * bexp + (size_t)u.pn * BM) * ldb); }
.LBB0_2359:
	s_mov_b32 s99, 0
	s_add_i32 s47, s47, 1
	s_mul_i32 s0, s47, s94
	s_add_i32 s36, s0, s68
	s_cmp_lt_i32 s36, s34
	s_cselect_b64 s[0:1], -1, 0
	s_ashr_i32 s30, s36, 2
	s_and_b32 s58, s36, 3
	s_ashr_i32 s31, s30, 31
	s_cmp_ge_i32 s36, s34
	s_cbranch_scc1 .LBB0_2361
	s_lshl_b64 s[100:101], s[30:31], 2
	s_add_u32 s100, s16, s100
	s_addc_u32 s101, s17, s101
	global_load_dword v234, v129, s[100:101] sc1
	s_mov_b32 s99, 1

;     __device__ __forceinline__ const char* bptr(const Unit& u) const { return (const char*)(Bt + (size_t)u.pn * BM * ldb); }
;     __device__ __forceinline__ const char* bptr(const Unit& u) const { return (const char*)(Bt + (size_t)u.pn * BM * ldb + koff(u)); }
;     __device__ bool next(int i, Unit& u) const { if (i >= 6) return false; int pm_ = pm; asm volatile("" : "+s"(pm_)); u.pm = pm_; u.pn = (i + (GB >> 3)) % 6; return true; }
;     __device__ __forceinline__ const char* bptr(const Unit& u) const { return (const char*)(Bt + (size_t)u.pn * BM * ldb + koff(u)); }
;     __device__ __forceinline__ const char* bptr(const Unit& u) const { const int g = u.pm / nM; return (const char*)(Bt + (size_t)g * sB + (size_t)u.pn * BM * ldb); }
;     __device__ bool next(int i, Unit& u) const { if (i >= nN) return false; int pm_ = pm; asm volatile("" : "+s"(pm_)); u.pm = pm_; u.pn = (i + (GB >> 3)) & (nN - 1); return true; }
;     __device__ __forceinline__ const char* bptr(const Unit& u) const { return (const char*)(Bt + (size_t)u.pn * BM * ldb); }
;     __device__ bool next(int i, Unit& u) const { const int L = i * G + c; if (L >= nunits) return false; u.pm = L >> 2; u.pn = L & 3; return true; }
;     __device__ __forceinline__ const char* bptr(const Unit& u) const { const int e = __hip_atomic_load(tiles + u.pm, __ATOMIC_RELAXED, __HIP_MEMORY_SCOPE_AGENT); return (const char*)(Bt + ((size_t)e * bexp + (size_t)u.pn * BM) * ldb); }
.LBB0_2362:
	s_cmp_eq_u32 s62, 0
	s_cbranch_scc0 .Lg2_nofix
	s_cmp_eq_u32 s99, 0
	s_cbranch_scc1 .Lg2_nofix
	v_readfirstlane_b32 s28, v234
	v_readlane_b32 s100, v242, 37
	v_readlane_b32 s101, v242, 38
	s_lshl_b32 s98, s58, 18
	s_ashr_i32 s29, s28, 31
	s_lshl_b64 s[28:29], s[28:29], 20
	s_add_u32 s28, s100, s28
	s_addc_u32 s29, s101, s29
	s_add_u32 s28, s28, s98
	s_addc_u32 s29, s29, 0
